# final-phase rewrite + MLA attention output tile staged through free LDS ring stage and written with 4 dwordx4 stores per wave instead of 64 dword stores
# baseline (speedup 1.0000x reference)
.LBB0_938:
	s_or_b64 exec, exec, s[12:13]
	s_waitcnt lgkmcnt(0)
	ds_read_b128 v[130:133], v198
	ds_read_b128 v[134:137], v198 offset:1024
	ds_read_b128 v[138:141], v198 offset:2048
	ds_read_b128 v[142:145], v198 offset:3072
	s_mov_b64 s[100:101], 0x2000
	v_lshl_add_u64 v[146:147], s[100:101], 0, v[200:201]
	v_lshl_add_u64 v[148:149], s[100:101], 0, v[146:147]
	v_lshl_add_u64 v[150:151], s[100:101], 0, v[148:149]
	s_waitcnt lgkmcnt(0)
	global_store_dwordx4 v[200:201], v[130:133], off
	global_store_dwordx4 v[146:147], v[134:137], off
	global_store_dwordx4 v[148:149], v[138:141], off
	global_store_dwordx4 v[150:151], v[142:145], off
	s_mov_b64 s[2:3], 0
	s_mov_b64 s[68:69], -1
	s_and_b64 vcc, exec, s[66:67]
	s_waitcnt vmcnt(63) expcnt(7) lgkmcnt(15)
	s_barrier
	s_cbranch_vccnz .LBB0_936

.LBB0_966:
	s_and_saveexec_b64 s[22:23], s[2:3]
	v_readlane_b32 s37, v255, 48
	ds_write_b32 v227, v230
	s_or_b64 exec, exec, s[22:23]
	s_waitcnt lgkmcnt(0)
	ds_read_b32 v68, v1
	s_lshl_b64 s[0:1], s[12:13], 10
	s_add_u32 s0, s74, s0
	v_lshl_or_b32 v202, v196, 12, v195
	s_addc_u32 s1, s75, s1
	s_waitcnt lgkmcnt(0)
	v_rcp_f32_e32 v68, v68
	v_and_b32_e32 v66, 3, v194
	v_cmp_eq_u32_e64 s[2:3], 0, v66
	v_lshl_add_u64 v[66:67], s[0:1], 0, v[202:203]
	v_and_b32_e32 v197, 63, v194
	v_lshrrev_b32_e32 v198, 3, v197
	v_and_b32_e32 v200, 7, v197
	v_lshlrev_b32_e32 v200, 4, v200
	v_lshl_or_b32 v200, v198, 10, v200
	v_mov_b32_e32 v201, 0
	v_lshl_add_u64 v[200:201], s[0:1], 0, v[200:201]
	v_lshrrev_b32_e32 v199, 6, v194
	v_lshrrev_b32_e32 v198, 2, v199
	v_lshlrev_b32_e32 v198, 15, v198
	v_lshl_add_u32 v199, v199, 12, v198
	v_add_u32_e32 v199, 0x8000, v199
	v_lshl_add_u32 v198, v197, 4, v199
	v_lshl_add_u32 v197, v196, 9, v199
	v_add_u32_e32 v197, v197, v195
	v_mul_f32_e32 v68, 0x42000000, v68
	v_mul_f32_e32 v50, v50, v68
	s_nop 1
	v_mov_b32_dpp v70, v50 quad_perm:[1,0,3,2] row_mask:0xf bank_mask:0xf bound_ctrl:1
	v_mov_b32_dpp v69, v50 quad_perm:[2,3,0,1] row_mask:0xf bank_mask:0xf bound_ctrl:1
	v_mov_b32_dpp v71, v50 quad_perm:[3,2,1,0] row_mask:0xf bank_mask:0xf bound_ctrl:1
	s_and_saveexec_b64 s[12:13], s[2:3]
	s_cbranch_execz .LBB0_970
	v_mov_b32_e32 v72, v203
	v_cvt_pk_fp8_f32 v72, v50, v70
	v_cvt_pk_fp8_f32 v72, v69, v71 op_sel:[0,0,1]
	ds_write_b32 v197, v72 offset:0
.LBB0_970:
	s_or_b64 exec, exec, s[12:13]
	v_mul_f32_e32 v34, v34, v68
	s_nop 1
	v_mov_b32_dpp v69, v34 quad_perm:[1,0,3,2] row_mask:0xf bank_mask:0xf bound_ctrl:1
	v_mov_b32_dpp v50, v34 quad_perm:[2,3,0,1] row_mask:0xf bank_mask:0xf bound_ctrl:1
	v_mov_b32_dpp v70, v34 quad_perm:[3,2,1,0] row_mask:0xf bank_mask:0xf bound_ctrl:1
	s_and_saveexec_b64 s[12:13], s[2:3]
	s_cbranch_execz .LBB0_972
	v_mov_b32_e32 v71, v203
	v_cvt_pk_fp8_f32 v71, v34, v69
	v_cvt_pk_fp8_f32 v71, v50, v70 op_sel:[0,0,1]
	ds_write_b32 v197, v71 offset:32
.LBB0_972:
	s_or_b64 exec, exec, s[12:13]
	v_mul_f32_e32 v18, v18, v68
	s_nop 1
	v_mov_b32_dpp v50, v18 quad_perm:[1,0,3,2] row_mask:0xf bank_mask:0xf bound_ctrl:1
	v_mov_b32_dpp v34, v18 quad_perm:[2,3,0,1] row_mask:0xf bank_mask:0xf bound_ctrl:1
	v_mov_b32_dpp v69, v18 quad_perm:[3,2,1,0] row_mask:0xf bank_mask:0xf bound_ctrl:1
	s_and_saveexec_b64 s[12:13], s[2:3]
	s_cbranch_execz .LBB0_974
	v_mov_b32_e32 v70, v203
	v_cvt_pk_fp8_f32 v70, v18, v50
	v_cvt_pk_fp8_f32 v70, v34, v69 op_sel:[0,0,1]
	ds_write_b32 v197, v70 offset:64
.LBB0_974:
	s_or_b64 exec, exec, s[12:13]
	v_mul_f32_e32 v2, v2, v68
	s_nop 1
	v_mov_b32_dpp v34, v2 quad_perm:[1,0,3,2] row_mask:0xf bank_mask:0xf bound_ctrl:1
	v_mov_b32_dpp v18, v2 quad_perm:[2,3,0,1] row_mask:0xf bank_mask:0xf bound_ctrl:1
	v_mov_b32_dpp v50, v2 quad_perm:[3,2,1,0] row_mask:0xf bank_mask:0xf bound_ctrl:1
	s_and_saveexec_b64 s[12:13], s[2:3]
	s_cbranch_execz .LBB0_976
	v_mov_b32_e32 v68, v203
	v_cvt_pk_fp8_f32 v68, v2, v34
	v_cvt_pk_fp8_f32 v68, v18, v50 op_sel:[0,0,1]
	ds_write_b32 v197, v68 offset:96
.LBB0_976:
	s_or_b64 exec, exec, s[12:13]
	ds_read_b32 v2, v1 offset:4
	s_waitcnt lgkmcnt(0)
	v_rcp_f32_e32 v2, v2
	s_nop 0
	v_mul_f32_e32 v2, 0x42000000, v2
	v_mul_f32_e32 v18, v51, v2
	s_nop 1
	v_mov_b32_dpp v50, v18 quad_perm:[1,0,3,2] row_mask:0xf bank_mask:0xf bound_ctrl:1
	v_mov_b32_dpp v34, v18 quad_perm:[2,3,0,1] row_mask:0xf bank_mask:0xf bound_ctrl:1
	v_mov_b32_dpp v51, v18 quad_perm:[3,2,1,0] row_mask:0xf bank_mask:0xf bound_ctrl:1
	s_and_saveexec_b64 s[12:13], s[2:3]
	s_cbranch_execz .LBB0_978
	v_mov_b32_e32 v68, v203
	v_cvt_pk_fp8_f32 v68, v18, v50
	v_cvt_pk_fp8_f32 v68, v34, v51 op_sel:[0,0,1]
	ds_write_b32 v197, v68 offset:128
.LBB0_978:
	s_or_b64 exec, exec, s[12:13]
	v_mul_f32_e32 v18, v35, v2
	s_nop 1
	v_mov_b32_dpp v35, v18 quad_perm:[1,0,3,2] row_mask:0xf bank_mask:0xf bound_ctrl:1
	v_mov_b32_dpp v34, v18 quad_perm:[2,3,0,1] row_mask:0xf bank_mask:0xf bound_ctrl:1
	v_mov_b32_dpp v50, v18 quad_perm:[3,2,1,0] row_mask:0xf bank_mask:0xf bound_ctrl:1
	s_and_saveexec_b64 s[12:13], s[2:3]
	s_cbranch_execz .LBB0_980
	v_mov_b32_e32 v51, v203
	v_cvt_pk_fp8_f32 v51, v18, v35
	v_cvt_pk_fp8_f32 v51, v34, v50 op_sel:[0,0,1]
	ds_write_b32 v197, v51 offset:160
.LBB0_980:
	s_or_b64 exec, exec, s[12:13]
	v_mul_f32_e32 v18, v19, v2
	s_nop 1
	v_mov_b32_dpp v34, v18 quad_perm:[1,0,3,2] row_mask:0xf bank_mask:0xf bound_ctrl:1
	v_mov_b32_dpp v19, v18 quad_perm:[2,3,0,1] row_mask:0xf bank_mask:0xf bound_ctrl:1
	v_mov_b32_dpp v35, v18 quad_perm:[3,2,1,0] row_mask:0xf bank_mask:0xf bound_ctrl:1
	s_and_saveexec_b64 s[12:13], s[2:3]
	s_cbranch_execz .LBB0_982
	v_mov_b32_e32 v50, v203
	v_cvt_pk_fp8_f32 v50, v18, v34
	v_cvt_pk_fp8_f32 v50, v19, v35 op_sel:[0,0,1]
	ds_write_b32 v197, v50 offset:192
.LBB0_982:
	s_or_b64 exec, exec, s[12:13]
	v_mul_f32_e32 v2, v3, v2
	s_nop 1
	v_mov_b32_dpp v18, v2 quad_perm:[1,0,3,2] row_mask:0xf bank_mask:0xf bound_ctrl:1
	v_mov_b32_dpp v3, v2 quad_perm:[2,3,0,1] row_mask:0xf bank_mask:0xf bound_ctrl:1
	v_mov_b32_dpp v19, v2 quad_perm:[3,2,1,0] row_mask:0xf bank_mask:0xf bound_ctrl:1
	s_and_saveexec_b64 s[12:13], s[2:3]
	s_cbranch_execz .LBB0_984
	v_mov_b32_e32 v34, v203
	v_cvt_pk_fp8_f32 v34, v2, v18
	v_cvt_pk_fp8_f32 v34, v3, v19 op_sel:[0,0,1]
	ds_write_b32 v197, v34 offset:224
.LBB0_984:
	s_or_b64 exec, exec, s[12:13]
	ds_read_b32 v2, v1 offset:8
	s_waitcnt lgkmcnt(0)
	v_rcp_f32_e32 v2, v2
	s_nop 0
	v_mul_f32_e32 v2, 0x42000000, v2
	v_mul_f32_e32 v3, v52, v2
	s_nop 1
	v_mov_b32_dpp v19, v3 quad_perm:[1,0,3,2] row_mask:0xf bank_mask:0xf bound_ctrl:1
	v_mov_b32_dpp v18, v3 quad_perm:[2,3,0,1] row_mask:0xf bank_mask:0xf bound_ctrl:1
	v_mov_b32_dpp v34, v3 quad_perm:[3,2,1,0] row_mask:0xf bank_mask:0xf bound_ctrl:1
	s_and_saveexec_b64 s[12:13], s[2:3]
	s_cbranch_execz .LBB0_986
	v_mov_b32_e32 v35, v203
	v_cvt_pk_fp8_f32 v35, v3, v19
	v_cvt_pk_fp8_f32 v35, v18, v34 op_sel:[0,0,1]
	ds_write_b32 v197, v35 offset:256
.LBB0_986:
	s_or_b64 exec, exec, s[12:13]
	v_mul_f32_e32 v3, v36, v2
	s_nop 1
	v_mov_b32_dpp v19, v3 quad_perm:[1,0,3,2] row_mask:0xf bank_mask:0xf bound_ctrl:1
	v_mov_b32_dpp v18, v3 quad_perm:[2,3,0,1] row_mask:0xf bank_mask:0xf bound_ctrl:1
	v_mov_b32_dpp v34, v3 quad_perm:[3,2,1,0] row_mask:0xf bank_mask:0xf bound_ctrl:1
	s_and_saveexec_b64 s[12:13], s[2:3]
	s_cbranch_execz .LBB0_988
	v_mov_b32_e32 v35, v203
	v_cvt_pk_fp8_f32 v35, v3, v19
	v_cvt_pk_fp8_f32 v35, v18, v34 op_sel:[0,0,1]
	ds_write_b32 v197, v35 offset:288
.LBB0_988:
	s_or_b64 exec, exec, s[12:13]
	v_mul_f32_e32 v3, v20, v2
	s_nop 1
	v_mov_b32_dpp v19, v3 quad_perm:[1,0,3,2] row_mask:0xf bank_mask:0xf bound_ctrl:1
	v_mov_b32_dpp v18, v3 quad_perm:[2,3,0,1] row_mask:0xf bank_mask:0xf bound_ctrl:1
	v_mov_b32_dpp v20, v3 quad_perm:[3,2,1,0] row_mask:0xf bank_mask:0xf bound_ctrl:1
	s_and_saveexec_b64 s[12:13], s[2:3]
	s_cbranch_execz .LBB0_990
	v_mov_b32_e32 v34, v203
	v_cvt_pk_fp8_f32 v34, v3, v19
	v_cvt_pk_fp8_f32 v34, v18, v20 op_sel:[0,0,1]
	ds_write_b32 v197, v34 offset:320
.LBB0_990:
	s_or_b64 exec, exec, s[12:13]
	v_mul_f32_e32 v2, v4, v2
	s_nop 1
	v_mov_b32_dpp v4, v2 quad_perm:[1,0,3,2] row_mask:0xf bank_mask:0xf bound_ctrl:1
	v_mov_b32_dpp v3, v2 quad_perm:[2,3,0,1] row_mask:0xf bank_mask:0xf bound_ctrl:1
	v_mov_b32_dpp v18, v2 quad_perm:[3,2,1,0] row_mask:0xf bank_mask:0xf bound_ctrl:1
	s_and_saveexec_b64 s[12:13], s[2:3]
	s_cbranch_execz .LBB0_992
	v_mov_b32_e32 v19, v203
	v_cvt_pk_fp8_f32 v19, v2, v4
	v_cvt_pk_fp8_f32 v19, v3, v18 op_sel:[0,0,1]
	ds_write_b32 v197, v19 offset:352
.LBB0_992:
	s_or_b64 exec, exec, s[12:13]
	ds_read_b32 v2, v1 offset:12
	s_waitcnt lgkmcnt(0)
	v_rcp_f32_e32 v2, v2
	s_nop 0
	v_mul_f32_e32 v2, 0x42000000, v2
	v_mul_f32_e32 v3, v53, v2
	s_nop 1
	v_mov_b32_dpp v18, v3 quad_perm:[1,0,3,2] row_mask:0xf bank_mask:0xf bound_ctrl:1
	v_mov_b32_dpp v4, v3 quad_perm:[2,3,0,1] row_mask:0xf bank_mask:0xf bound_ctrl:1
	v_mov_b32_dpp v19, v3 quad_perm:[3,2,1,0] row_mask:0xf bank_mask:0xf bound_ctrl:1
	s_and_saveexec_b64 s[12:13], s[2:3]
	s_cbranch_execz .LBB0_994
	v_mov_b32_e32 v20, v203
	v_cvt_pk_fp8_f32 v20, v3, v18
	v_cvt_pk_fp8_f32 v20, v4, v19 op_sel:[0,0,1]
	ds_write_b32 v197, v20 offset:384
.LBB0_994:
	s_or_b64 exec, exec, s[12:13]
	v_mul_f32_e32 v3, v37, v2
	s_nop 1
	v_mov_b32_dpp v18, v3 quad_perm:[1,0,3,2] row_mask:0xf bank_mask:0xf bound_ctrl:1
	v_mov_b32_dpp v4, v3 quad_perm:[2,3,0,1] row_mask:0xf bank_mask:0xf bound_ctrl:1
	v_mov_b32_dpp v19, v3 quad_perm:[3,2,1,0] row_mask:0xf bank_mask:0xf bound_ctrl:1
	s_and_saveexec_b64 s[12:13], s[2:3]
	s_cbranch_execz .LBB0_996
	v_mov_b32_e32 v20, v203
	v_cvt_pk_fp8_f32 v20, v3, v18
	v_cvt_pk_fp8_f32 v20, v4, v19 op_sel:[0,0,1]
	ds_write_b32 v197, v20 offset:416
.LBB0_996:
	s_or_b64 exec, exec, s[12:13]
	v_mul_f32_e32 v3, v21, v2
	s_nop 1
	v_mov_b32_dpp v18, v3 quad_perm:[1,0,3,2] row_mask:0xf bank_mask:0xf bound_ctrl:1
	v_mov_b32_dpp v4, v3 quad_perm:[2,3,0,1] row_mask:0xf bank_mask:0xf bound_ctrl:1
	v_mov_b32_dpp v19, v3 quad_perm:[3,2,1,0] row_mask:0xf bank_mask:0xf bound_ctrl:1
	s_and_saveexec_b64 s[12:13], s[2:3]
	s_cbranch_execz .LBB0_998
	v_mov_b32_e32 v20, v203
	v_cvt_pk_fp8_f32 v20, v3, v18
	v_cvt_pk_fp8_f32 v20, v4, v19 op_sel:[0,0,1]
	ds_write_b32 v197, v20 offset:448
.LBB0_998:
	s_or_b64 exec, exec, s[12:13]
	v_mul_f32_e32 v2, v5, v2
	s_nop 1
	v_mov_b32_dpp v4, v2 quad_perm:[1,0,3,2] row_mask:0xf bank_mask:0xf bound_ctrl:1
	v_mov_b32_dpp v3, v2 quad_perm:[2,3,0,1] row_mask:0xf bank_mask:0xf bound_ctrl:1
	v_mov_b32_dpp v5, v2 quad_perm:[3,2,1,0] row_mask:0xf bank_mask:0xf bound_ctrl:1
	s_and_saveexec_b64 s[12:13], s[2:3]
	s_cbranch_execz .LBB0_1000
	v_mov_b32_e32 v18, v203
	v_cvt_pk_fp8_f32 v18, v2, v4
	v_cvt_pk_fp8_f32 v18, v3, v5 op_sel:[0,0,1]
	ds_write_b32 v197, v18 offset:480
.LBB0_1000:
	s_or_b64 exec, exec, s[12:13]
	ds_read_b32 v2, v1 offset:32
	s_waitcnt lgkmcnt(0)
	v_rcp_f32_e32 v2, v2
	s_nop 0
	v_mul_f32_e32 v2, 0x42000000, v2
	v_mul_f32_e32 v3, v54, v2
	s_nop 1
	v_mov_b32_dpp v5, v3 quad_perm:[1,0,3,2] row_mask:0xf bank_mask:0xf bound_ctrl:1
	v_mov_b32_dpp v4, v3 quad_perm:[2,3,0,1] row_mask:0xf bank_mask:0xf bound_ctrl:1
	v_mov_b32_dpp v18, v3 quad_perm:[3,2,1,0] row_mask:0xf bank_mask:0xf bound_ctrl:1
	s_and_saveexec_b64 s[12:13], s[2:3]
	s_cbranch_execz .LBB0_1002
	v_mov_b32_e32 v19, v203
	v_cvt_pk_fp8_f32 v19, v3, v5
	v_cvt_pk_fp8_f32 v19, v4, v18 op_sel:[0,0,1]
	v_add_co_u32_e32 v4, vcc, 0x2000, v66
	s_nop 1
	v_addc_co_u32_e32 v5, vcc, 0, v67, vcc
	ds_write_b32 v197, v19 offset:1024
.LBB0_1002:
	s_or_b64 exec, exec, s[12:13]
	v_mul_f32_e32 v3, v38, v2
	s_nop 1
	v_mov_b32_dpp v5, v3 quad_perm:[1,0,3,2] row_mask:0xf bank_mask:0xf bound_ctrl:1
	v_mov_b32_dpp v4, v3 quad_perm:[2,3,0,1] row_mask:0xf bank_mask:0xf bound_ctrl:1
	v_mov_b32_dpp v18, v3 quad_perm:[3,2,1,0] row_mask:0xf bank_mask:0xf bound_ctrl:1
	s_and_saveexec_b64 s[12:13], s[2:3]
	s_cbranch_execz .LBB0_1004
	v_mov_b32_e32 v19, v203
	v_cvt_pk_fp8_f32 v19, v3, v5
	v_cvt_pk_fp8_f32 v19, v4, v18 op_sel:[0,0,1]
	v_add_co_u32_e32 v4, vcc, 0x2000, v66
	s_nop 1
	v_addc_co_u32_e32 v5, vcc, 0, v67, vcc
	ds_write_b32 v197, v19 offset:1056
.LBB0_1004:
	s_or_b64 exec, exec, s[12:13]
	v_mul_f32_e32 v3, v22, v2
	s_nop 1
	v_mov_b32_dpp v5, v3 quad_perm:[1,0,3,2] row_mask:0xf bank_mask:0xf bound_ctrl:1
	v_mov_b32_dpp v4, v3 quad_perm:[2,3,0,1] row_mask:0xf bank_mask:0xf bound_ctrl:1
	v_mov_b32_dpp v18, v3 quad_perm:[3,2,1,0] row_mask:0xf bank_mask:0xf bound_ctrl:1
	s_and_saveexec_b64 s[12:13], s[2:3]
	s_cbranch_execz .LBB0_1006
	v_mov_b32_e32 v19, v203
	v_cvt_pk_fp8_f32 v19, v3, v5
	v_cvt_pk_fp8_f32 v19, v4, v18 op_sel:[0,0,1]
	v_add_co_u32_e32 v4, vcc, 0x2000, v66
	s_nop 1
	v_addc_co_u32_e32 v5, vcc, 0, v67, vcc
	ds_write_b32 v197, v19 offset:1088
.LBB0_1006:
	s_or_b64 exec, exec, s[12:13]
	v_mul_f32_e32 v2, v6, v2
	s_nop 1
	v_mov_b32_dpp v4, v2 quad_perm:[1,0,3,2] row_mask:0xf bank_mask:0xf bound_ctrl:1
	v_mov_b32_dpp v3, v2 quad_perm:[2,3,0,1] row_mask:0xf bank_mask:0xf bound_ctrl:1
	v_mov_b32_dpp v5, v2 quad_perm:[3,2,1,0] row_mask:0xf bank_mask:0xf bound_ctrl:1
	s_and_saveexec_b64 s[12:13], s[2:3]
	s_cbranch_execz .LBB0_1008
	v_mov_b32_e32 v6, v203
	v_cvt_pk_fp8_f32 v6, v2, v4
	v_add_co_u32_e32 v2, vcc, 0x2000, v66
	v_cvt_pk_fp8_f32 v6, v3, v5 op_sel:[0,0,1]
	s_nop 0
	v_addc_co_u32_e32 v3, vcc, 0, v67, vcc
	ds_write_b32 v197, v6 offset:1120
.LBB0_1008:
	s_or_b64 exec, exec, s[12:13]
	ds_read_b32 v2, v1 offset:36
	s_waitcnt lgkmcnt(0)
	v_rcp_f32_e32 v2, v2
	s_nop 0
	v_mul_f32_e32 v2, 0x42000000, v2
	v_mul_f32_e32 v3, v55, v2
	s_nop 1
	v_mov_b32_dpp v5, v3 quad_perm:[1,0,3,2] row_mask:0xf bank_mask:0xf bound_ctrl:1
	v_mov_b32_dpp v4, v3 quad_perm:[2,3,0,1] row_mask:0xf bank_mask:0xf bound_ctrl:1
	v_mov_b32_dpp v6, v3 quad_perm:[3,2,1,0] row_mask:0xf bank_mask:0xf bound_ctrl:1
	s_and_saveexec_b64 s[12:13], s[2:3]
	s_cbranch_execz .LBB0_1010
	v_mov_b32_e32 v18, v203
	v_cvt_pk_fp8_f32 v18, v3, v5
	v_cvt_pk_fp8_f32 v18, v4, v6 op_sel:[0,0,1]
	v_add_co_u32_e32 v4, vcc, 0x2000, v66
	s_nop 1
	v_addc_co_u32_e32 v5, vcc, 0, v67, vcc
	ds_write_b32 v197, v18 offset:1152
.LBB0_1010:
	s_or_b64 exec, exec, s[12:13]
	v_mul_f32_e32 v3, v39, v2
	s_nop 1
	v_mov_b32_dpp v5, v3 quad_perm:[1,0,3,2] row_mask:0xf bank_mask:0xf bound_ctrl:1
	v_mov_b32_dpp v4, v3 quad_perm:[2,3,0,1] row_mask:0xf bank_mask:0xf bound_ctrl:1
	v_mov_b32_dpp v6, v3 quad_perm:[3,2,1,0] row_mask:0xf bank_mask:0xf bound_ctrl:1
	s_and_saveexec_b64 s[12:13], s[2:3]
	s_cbranch_execz .LBB0_1012
	v_mov_b32_e32 v18, v203
	v_cvt_pk_fp8_f32 v18, v3, v5
	v_cvt_pk_fp8_f32 v18, v4, v6 op_sel:[0,0,1]
	v_add_co_u32_e32 v4, vcc, 0x2000, v66
	s_nop 1
	v_addc_co_u32_e32 v5, vcc, 0, v67, vcc
	ds_write_b32 v197, v18 offset:1184
.LBB0_1012:
	s_or_b64 exec, exec, s[12:13]
	v_mul_f32_e32 v3, v23, v2
	s_nop 1
	v_mov_b32_dpp v5, v3 quad_perm:[1,0,3,2] row_mask:0xf bank_mask:0xf bound_ctrl:1
	v_mov_b32_dpp v4, v3 quad_perm:[2,3,0,1] row_mask:0xf bank_mask:0xf bound_ctrl:1
	v_mov_b32_dpp v6, v3 quad_perm:[3,2,1,0] row_mask:0xf bank_mask:0xf bound_ctrl:1
	s_and_saveexec_b64 s[12:13], s[2:3]
	s_cbranch_execz .LBB0_1014
	v_mov_b32_e32 v18, v203
	v_cvt_pk_fp8_f32 v18, v3, v5
	v_cvt_pk_fp8_f32 v18, v4, v6 op_sel:[0,0,1]
	v_add_co_u32_e32 v4, vcc, 0x2000, v66
	s_nop 1
	v_addc_co_u32_e32 v5, vcc, 0, v67, vcc
	ds_write_b32 v197, v18 offset:1216
.LBB0_1014:
	s_or_b64 exec, exec, s[12:13]
	v_mul_f32_e32 v2, v7, v2
	s_nop 1
	v_mov_b32_dpp v4, v2 quad_perm:[1,0,3,2] row_mask:0xf bank_mask:0xf bound_ctrl:1
	v_mov_b32_dpp v3, v2 quad_perm:[2,3,0,1] row_mask:0xf bank_mask:0xf bound_ctrl:1
	v_mov_b32_dpp v5, v2 quad_perm:[3,2,1,0] row_mask:0xf bank_mask:0xf bound_ctrl:1
	s_and_saveexec_b64 s[12:13], s[2:3]
	s_cbranch_execz .LBB0_1016
	v_mov_b32_e32 v6, v203
	v_cvt_pk_fp8_f32 v6, v2, v4
	v_add_co_u32_e32 v2, vcc, 0x2000, v66
	v_cvt_pk_fp8_f32 v6, v3, v5 op_sel:[0,0,1]
	s_nop 0
	v_addc_co_u32_e32 v3, vcc, 0, v67, vcc
	ds_write_b32 v197, v6 offset:1248
.LBB0_1016:
	s_or_b64 exec, exec, s[12:13]
	ds_read_b32 v2, v1 offset:40
	s_waitcnt lgkmcnt(0)
	v_rcp_f32_e32 v2, v2
	s_nop 0
	v_mul_f32_e32 v2, 0x42000000, v2
	v_mul_f32_e32 v3, v56, v2
	s_nop 1
	v_mov_b32_dpp v5, v3 quad_perm:[1,0,3,2] row_mask:0xf bank_mask:0xf bound_ctrl:1
	v_mov_b32_dpp v4, v3 quad_perm:[2,3,0,1] row_mask:0xf bank_mask:0xf bound_ctrl:1
	v_mov_b32_dpp v6, v3 quad_perm:[3,2,1,0] row_mask:0xf bank_mask:0xf bound_ctrl:1
	s_and_saveexec_b64 s[12:13], s[2:3]
	s_cbranch_execz .LBB0_1018
	v_mov_b32_e32 v7, v203
	v_cvt_pk_fp8_f32 v7, v3, v5
	v_cvt_pk_fp8_f32 v7, v4, v6 op_sel:[0,0,1]
	v_add_co_u32_e32 v4, vcc, 0x2000, v66
	s_nop 1
	v_addc_co_u32_e32 v5, vcc, 0, v67, vcc
	ds_write_b32 v197, v7 offset:1280
.LBB0_1018:
	s_or_b64 exec, exec, s[12:13]
	v_mul_f32_e32 v3, v40, v2
	s_nop 1
	v_mov_b32_dpp v5, v3 quad_perm:[1,0,3,2] row_mask:0xf bank_mask:0xf bound_ctrl:1
	v_mov_b32_dpp v4, v3 quad_perm:[2,3,0,1] row_mask:0xf bank_mask:0xf bound_ctrl:1
	v_mov_b32_dpp v6, v3 quad_perm:[3,2,1,0] row_mask:0xf bank_mask:0xf bound_ctrl:1
	s_and_saveexec_b64 s[12:13], s[2:3]
	s_cbranch_execz .LBB0_1020
	v_mov_b32_e32 v7, v203
	v_cvt_pk_fp8_f32 v7, v3, v5
	v_cvt_pk_fp8_f32 v7, v4, v6 op_sel:[0,0,1]
	v_add_co_u32_e32 v4, vcc, 0x2000, v66
	s_nop 1
	v_addc_co_u32_e32 v5, vcc, 0, v67, vcc
	ds_write_b32 v197, v7 offset:1312
.LBB0_1020:
	s_or_b64 exec, exec, s[12:13]
	v_mul_f32_e32 v3, v24, v2
	s_nop 1
	v_mov_b32_dpp v5, v3 quad_perm:[1,0,3,2] row_mask:0xf bank_mask:0xf bound_ctrl:1
	v_mov_b32_dpp v4, v3 quad_perm:[2,3,0,1] row_mask:0xf bank_mask:0xf bound_ctrl:1
	v_mov_b32_dpp v6, v3 quad_perm:[3,2,1,0] row_mask:0xf bank_mask:0xf bound_ctrl:1
	s_and_saveexec_b64 s[12:13], s[2:3]
	s_cbranch_execz .LBB0_1022
	v_mov_b32_e32 v7, v203
	v_cvt_pk_fp8_f32 v7, v3, v5
	v_cvt_pk_fp8_f32 v7, v4, v6 op_sel:[0,0,1]
	v_add_co_u32_e32 v4, vcc, 0x2000, v66
	s_nop 1
	v_addc_co_u32_e32 v5, vcc, 0, v67, vcc
	ds_write_b32 v197, v7 offset:1344
.LBB0_1022:
	s_or_b64 exec, exec, s[12:13]
	v_mul_f32_e32 v2, v8, v2
	s_nop 1
	v_mov_b32_dpp v4, v2 quad_perm:[1,0,3,2] row_mask:0xf bank_mask:0xf bound_ctrl:1
	v_mov_b32_dpp v3, v2 quad_perm:[2,3,0,1] row_mask:0xf bank_mask:0xf bound_ctrl:1
	v_mov_b32_dpp v5, v2 quad_perm:[3,2,1,0] row_mask:0xf bank_mask:0xf bound_ctrl:1
	s_and_saveexec_b64 s[12:13], s[2:3]
	s_cbranch_execz .LBB0_1024
	v_mov_b32_e32 v6, v203
	v_cvt_pk_fp8_f32 v6, v2, v4
	v_add_co_u32_e32 v2, vcc, 0x2000, v66
	v_cvt_pk_fp8_f32 v6, v3, v5 op_sel:[0,0,1]
	s_nop 0
	v_addc_co_u32_e32 v3, vcc, 0, v67, vcc
	ds_write_b32 v197, v6 offset:1376
.LBB0_1024:
	s_or_b64 exec, exec, s[12:13]
	ds_read_b32 v2, v1 offset:44
	s_waitcnt lgkmcnt(0)
	v_rcp_f32_e32 v2, v2
	s_nop 0
	v_mul_f32_e32 v2, 0x42000000, v2
	v_mul_f32_e32 v3, v57, v2
	s_nop 1
	v_mov_b32_dpp v5, v3 quad_perm:[1,0,3,2] row_mask:0xf bank_mask:0xf bound_ctrl:1
	v_mov_b32_dpp v4, v3 quad_perm:[2,3,0,1] row_mask:0xf bank_mask:0xf bound_ctrl:1
	v_mov_b32_dpp v6, v3 quad_perm:[3,2,1,0] row_mask:0xf bank_mask:0xf bound_ctrl:1
	s_and_saveexec_b64 s[12:13], s[2:3]
	s_cbranch_execz .LBB0_1026
	v_mov_b32_e32 v7, v203
	v_cvt_pk_fp8_f32 v7, v3, v5
	v_cvt_pk_fp8_f32 v7, v4, v6 op_sel:[0,0,1]
	v_add_co_u32_e32 v4, vcc, 0x2000, v66
	s_nop 1
	v_addc_co_u32_e32 v5, vcc, 0, v67, vcc
	ds_write_b32 v197, v7 offset:1408
.LBB0_1026:
	s_or_b64 exec, exec, s[12:13]
	v_mul_f32_e32 v3, v41, v2
	s_nop 1
	v_mov_b32_dpp v5, v3 quad_perm:[1,0,3,2] row_mask:0xf bank_mask:0xf bound_ctrl:1
	v_mov_b32_dpp v4, v3 quad_perm:[2,3,0,1] row_mask:0xf bank_mask:0xf bound_ctrl:1
	v_mov_b32_dpp v6, v3 quad_perm:[3,2,1,0] row_mask:0xf bank_mask:0xf bound_ctrl:1
	s_and_saveexec_b64 s[12:13], s[2:3]
	s_cbranch_execz .LBB0_1028
	v_mov_b32_e32 v7, v203
	v_cvt_pk_fp8_f32 v7, v3, v5
	v_cvt_pk_fp8_f32 v7, v4, v6 op_sel:[0,0,1]
	v_add_co_u32_e32 v4, vcc, 0x2000, v66
	s_nop 1
	v_addc_co_u32_e32 v5, vcc, 0, v67, vcc
	ds_write_b32 v197, v7 offset:1440
.LBB0_1028:
	s_or_b64 exec, exec, s[12:13]
	v_mul_f32_e32 v3, v25, v2
	s_nop 1
	v_mov_b32_dpp v5, v3 quad_perm:[1,0,3,2] row_mask:0xf bank_mask:0xf bound_ctrl:1
	v_mov_b32_dpp v4, v3 quad_perm:[2,3,0,1] row_mask:0xf bank_mask:0xf bound_ctrl:1
	v_mov_b32_dpp v6, v3 quad_perm:[3,2,1,0] row_mask:0xf bank_mask:0xf bound_ctrl:1
	s_and_saveexec_b64 s[12:13], s[2:3]
	s_cbranch_execz .LBB0_1030
	v_mov_b32_e32 v7, v203
	v_cvt_pk_fp8_f32 v7, v3, v5
	v_cvt_pk_fp8_f32 v7, v4, v6 op_sel:[0,0,1]
	v_add_co_u32_e32 v4, vcc, 0x2000, v66
	s_nop 1
	v_addc_co_u32_e32 v5, vcc, 0, v67, vcc
	ds_write_b32 v197, v7 offset:1472
.LBB0_1030:
	s_or_b64 exec, exec, s[12:13]
	v_mul_f32_e32 v2, v9, v2
	s_nop 1
	v_mov_b32_dpp v4, v2 quad_perm:[1,0,3,2] row_mask:0xf bank_mask:0xf bound_ctrl:1
	v_mov_b32_dpp v3, v2 quad_perm:[2,3,0,1] row_mask:0xf bank_mask:0xf bound_ctrl:1
	v_mov_b32_dpp v5, v2 quad_perm:[3,2,1,0] row_mask:0xf bank_mask:0xf bound_ctrl:1
	s_and_saveexec_b64 s[12:13], s[2:3]
	s_cbranch_execz .LBB0_1032
	v_mov_b32_e32 v6, v203
	v_cvt_pk_fp8_f32 v6, v2, v4
	v_add_co_u32_e32 v2, vcc, 0x2000, v66
	v_cvt_pk_fp8_f32 v6, v3, v5 op_sel:[0,0,1]
	s_nop 0
	v_addc_co_u32_e32 v3, vcc, 0, v67, vcc
	ds_write_b32 v197, v6 offset:1504
.LBB0_1032:
	s_or_b64 exec, exec, s[12:13]
	ds_read_b32 v2, v1 offset:64
	s_waitcnt lgkmcnt(0)
	v_rcp_f32_e32 v2, v2
	s_nop 0
	v_mul_f32_e32 v2, 0x42000000, v2
	v_mul_f32_e32 v3, v58, v2
	s_nop 1
	v_mov_b32_dpp v5, v3 quad_perm:[1,0,3,2] row_mask:0xf bank_mask:0xf bound_ctrl:1
	v_mov_b32_dpp v4, v3 quad_perm:[2,3,0,1] row_mask:0xf bank_mask:0xf bound_ctrl:1
	v_mov_b32_dpp v6, v3 quad_perm:[3,2,1,0] row_mask:0xf bank_mask:0xf bound_ctrl:1
	s_and_saveexec_b64 s[12:13], s[2:3]
	s_cbranch_execz .LBB0_1034
	v_mov_b32_e32 v7, v203
	v_cvt_pk_fp8_f32 v7, v3, v5
	v_cvt_pk_fp8_f32 v7, v4, v6 op_sel:[0,0,1]
	v_add_co_u32_e32 v4, vcc, 0x4000, v66
	s_nop 1
	v_addc_co_u32_e32 v5, vcc, 0, v67, vcc
	ds_write_b32 v197, v7 offset:2048
.LBB0_1034:
	s_or_b64 exec, exec, s[12:13]
	v_mul_f32_e32 v3, v42, v2
	s_nop 1
	v_mov_b32_dpp v5, v3 quad_perm:[1,0,3,2] row_mask:0xf bank_mask:0xf bound_ctrl:1
	v_mov_b32_dpp v4, v3 quad_perm:[2,3,0,1] row_mask:0xf bank_mask:0xf bound_ctrl:1
	v_mov_b32_dpp v6, v3 quad_perm:[3,2,1,0] row_mask:0xf bank_mask:0xf bound_ctrl:1
	s_and_saveexec_b64 s[12:13], s[2:3]
	s_cbranch_execz .LBB0_1036
	v_mov_b32_e32 v7, v203
	v_cvt_pk_fp8_f32 v7, v3, v5
	v_cvt_pk_fp8_f32 v7, v4, v6 op_sel:[0,0,1]
	v_add_co_u32_e32 v4, vcc, 0x4000, v66
	s_nop 1
	v_addc_co_u32_e32 v5, vcc, 0, v67, vcc
	ds_write_b32 v197, v7 offset:2080
.LBB0_1036:
	s_or_b64 exec, exec, s[12:13]
	v_mul_f32_e32 v3, v26, v2
	s_nop 1
	v_mov_b32_dpp v5, v3 quad_perm:[1,0,3,2] row_mask:0xf bank_mask:0xf bound_ctrl:1
	v_mov_b32_dpp v4, v3 quad_perm:[2,3,0,1] row_mask:0xf bank_mask:0xf bound_ctrl:1
	v_mov_b32_dpp v6, v3 quad_perm:[3,2,1,0] row_mask:0xf bank_mask:0xf bound_ctrl:1
	s_and_saveexec_b64 s[12:13], s[2:3]
	s_cbranch_execz .LBB0_1038
	v_mov_b32_e32 v7, v203
	v_cvt_pk_fp8_f32 v7, v3, v5
	v_cvt_pk_fp8_f32 v7, v4, v6 op_sel:[0,0,1]
	v_add_co_u32_e32 v4, vcc, 0x4000, v66
	s_nop 1
	v_addc_co_u32_e32 v5, vcc, 0, v67, vcc
	ds_write_b32 v197, v7 offset:2112
.LBB0_1038:
	s_or_b64 exec, exec, s[12:13]
	v_mul_f32_e32 v2, v10, v2
	s_nop 1
	v_mov_b32_dpp v4, v2 quad_perm:[1,0,3,2] row_mask:0xf bank_mask:0xf bound_ctrl:1
	v_mov_b32_dpp v3, v2 quad_perm:[2,3,0,1] row_mask:0xf bank_mask:0xf bound_ctrl:1
	v_mov_b32_dpp v5, v2 quad_perm:[3,2,1,0] row_mask:0xf bank_mask:0xf bound_ctrl:1
	s_and_saveexec_b64 s[12:13], s[2:3]
	s_cbranch_execz .LBB0_1040
	v_mov_b32_e32 v6, v203
	v_cvt_pk_fp8_f32 v6, v2, v4
	v_add_co_u32_e32 v2, vcc, 0x4000, v66
	v_cvt_pk_fp8_f32 v6, v3, v5 op_sel:[0,0,1]
	s_nop 0
	v_addc_co_u32_e32 v3, vcc, 0, v67, vcc
	ds_write_b32 v197, v6 offset:2144
.LBB0_1040:
	s_or_b64 exec, exec, s[12:13]
	ds_read_b32 v2, v1 offset:68
	s_waitcnt lgkmcnt(0)
	v_rcp_f32_e32 v2, v2
	s_nop 0
	v_mul_f32_e32 v2, 0x42000000, v2
	v_mul_f32_e32 v3, v59, v2
	s_nop 1
	v_mov_b32_dpp v5, v3 quad_perm:[1,0,3,2] row_mask:0xf bank_mask:0xf bound_ctrl:1
	v_mov_b32_dpp v4, v3 quad_perm:[2,3,0,1] row_mask:0xf bank_mask:0xf bound_ctrl:1
	v_mov_b32_dpp v6, v3 quad_perm:[3,2,1,0] row_mask:0xf bank_mask:0xf bound_ctrl:1
	s_and_saveexec_b64 s[12:13], s[2:3]
	s_cbranch_execz .LBB0_1042
	v_mov_b32_e32 v7, v203
	v_cvt_pk_fp8_f32 v7, v3, v5
	v_cvt_pk_fp8_f32 v7, v4, v6 op_sel:[0,0,1]
	v_add_co_u32_e32 v4, vcc, 0x4000, v66
	s_nop 1
	v_addc_co_u32_e32 v5, vcc, 0, v67, vcc
	ds_write_b32 v197, v7 offset:2176
.LBB0_1042:
	s_or_b64 exec, exec, s[12:13]
	v_mul_f32_e32 v3, v43, v2
	s_nop 1
	v_mov_b32_dpp v5, v3 quad_perm:[1,0,3,2] row_mask:0xf bank_mask:0xf bound_ctrl:1
	v_mov_b32_dpp v4, v3 quad_perm:[2,3,0,1] row_mask:0xf bank_mask:0xf bound_ctrl:1
	v_mov_b32_dpp v6, v3 quad_perm:[3,2,1,0] row_mask:0xf bank_mask:0xf bound_ctrl:1
	s_and_saveexec_b64 s[12:13], s[2:3]
	s_cbranch_execz .LBB0_1044
	v_mov_b32_e32 v7, v203
	v_cvt_pk_fp8_f32 v7, v3, v5
	v_cvt_pk_fp8_f32 v7, v4, v6 op_sel:[0,0,1]
	v_add_co_u32_e32 v4, vcc, 0x4000, v66
	s_nop 1
	v_addc_co_u32_e32 v5, vcc, 0, v67, vcc
	ds_write_b32 v197, v7 offset:2208
.LBB0_1044:
	s_or_b64 exec, exec, s[12:13]
	v_mul_f32_e32 v3, v27, v2
	s_nop 1
	v_mov_b32_dpp v5, v3 quad_perm:[1,0,3,2] row_mask:0xf bank_mask:0xf bound_ctrl:1
	v_mov_b32_dpp v4, v3 quad_perm:[2,3,0,1] row_mask:0xf bank_mask:0xf bound_ctrl:1
	v_mov_b32_dpp v6, v3 quad_perm:[3,2,1,0] row_mask:0xf bank_mask:0xf bound_ctrl:1
	s_and_saveexec_b64 s[12:13], s[2:3]
	s_cbranch_execz .LBB0_1046
	v_mov_b32_e32 v7, v203
	v_cvt_pk_fp8_f32 v7, v3, v5
	v_cvt_pk_fp8_f32 v7, v4, v6 op_sel:[0,0,1]
	v_add_co_u32_e32 v4, vcc, 0x4000, v66
	s_nop 1
	v_addc_co_u32_e32 v5, vcc, 0, v67, vcc
	ds_write_b32 v197, v7 offset:2240
.LBB0_1046:
	s_or_b64 exec, exec, s[12:13]
	v_mul_f32_e32 v2, v11, v2
	s_nop 1
	v_mov_b32_dpp v4, v2 quad_perm:[1,0,3,2] row_mask:0xf bank_mask:0xf bound_ctrl:1
	v_mov_b32_dpp v3, v2 quad_perm:[2,3,0,1] row_mask:0xf bank_mask:0xf bound_ctrl:1
	v_mov_b32_dpp v5, v2 quad_perm:[3,2,1,0] row_mask:0xf bank_mask:0xf bound_ctrl:1
	s_and_saveexec_b64 s[12:13], s[2:3]
	s_cbranch_execz .LBB0_1048
	v_mov_b32_e32 v6, v203
	v_cvt_pk_fp8_f32 v6, v2, v4
	v_add_co_u32_e32 v2, vcc, 0x4000, v66
	v_cvt_pk_fp8_f32 v6, v3, v5 op_sel:[0,0,1]
	s_nop 0
	v_addc_co_u32_e32 v3, vcc, 0, v67, vcc
	ds_write_b32 v197, v6 offset:2272
.LBB0_1048:
	s_or_b64 exec, exec, s[12:13]
	ds_read_b32 v2, v1 offset:72
	s_waitcnt lgkmcnt(0)
	v_rcp_f32_e32 v2, v2
	s_nop 0
	v_mul_f32_e32 v2, 0x42000000, v2
	v_mul_f32_e32 v3, v60, v2
	s_nop 1
	v_mov_b32_dpp v5, v3 quad_perm:[1,0,3,2] row_mask:0xf bank_mask:0xf bound_ctrl:1
	v_mov_b32_dpp v4, v3 quad_perm:[2,3,0,1] row_mask:0xf bank_mask:0xf bound_ctrl:1
	v_mov_b32_dpp v6, v3 quad_perm:[3,2,1,0] row_mask:0xf bank_mask:0xf bound_ctrl:1
	s_and_saveexec_b64 s[12:13], s[2:3]
	s_cbranch_execz .LBB0_1050
	v_mov_b32_e32 v7, v203
	v_cvt_pk_fp8_f32 v7, v3, v5
	v_cvt_pk_fp8_f32 v7, v4, v6 op_sel:[0,0,1]
	v_add_co_u32_e32 v4, vcc, 0x4000, v66
	s_nop 1
	v_addc_co_u32_e32 v5, vcc, 0, v67, vcc
	ds_write_b32 v197, v7 offset:2304
.LBB0_1050:
	s_or_b64 exec, exec, s[12:13]
	v_mul_f32_e32 v3, v44, v2
	s_nop 1
	v_mov_b32_dpp v5, v3 quad_perm:[1,0,3,2] row_mask:0xf bank_mask:0xf bound_ctrl:1
	v_mov_b32_dpp v4, v3 quad_perm:[2,3,0,1] row_mask:0xf bank_mask:0xf bound_ctrl:1
	v_mov_b32_dpp v6, v3 quad_perm:[3,2,1,0] row_mask:0xf bank_mask:0xf bound_ctrl:1
	s_and_saveexec_b64 s[12:13], s[2:3]
	s_cbranch_execz .LBB0_1052
	v_mov_b32_e32 v7, v203
	v_cvt_pk_fp8_f32 v7, v3, v5
	v_cvt_pk_fp8_f32 v7, v4, v6 op_sel:[0,0,1]
	v_add_co_u32_e32 v4, vcc, 0x4000, v66
	s_nop 1
	v_addc_co_u32_e32 v5, vcc, 0, v67, vcc
	ds_write_b32 v197, v7 offset:2336
.LBB0_1052:
	s_or_b64 exec, exec, s[12:13]
	v_mul_f32_e32 v3, v28, v2
	s_nop 1
	v_mov_b32_dpp v5, v3 quad_perm:[1,0,3,2] row_mask:0xf bank_mask:0xf bound_ctrl:1
	v_mov_b32_dpp v4, v3 quad_perm:[2,3,0,1] row_mask:0xf bank_mask:0xf bound_ctrl:1
	v_mov_b32_dpp v6, v3 quad_perm:[3,2,1,0] row_mask:0xf bank_mask:0xf bound_ctrl:1
	s_and_saveexec_b64 s[12:13], s[2:3]
	s_cbranch_execz .LBB0_1054
	v_mov_b32_e32 v7, v203
	v_cvt_pk_fp8_f32 v7, v3, v5
	v_cvt_pk_fp8_f32 v7, v4, v6 op_sel:[0,0,1]
	v_add_co_u32_e32 v4, vcc, 0x4000, v66
	s_nop 1
	v_addc_co_u32_e32 v5, vcc, 0, v67, vcc
	ds_write_b32 v197, v7 offset:2368
.LBB0_1054:
	s_or_b64 exec, exec, s[12:13]
	v_mul_f32_e32 v2, v12, v2
	s_nop 1
	v_mov_b32_dpp v4, v2 quad_perm:[1,0,3,2] row_mask:0xf bank_mask:0xf bound_ctrl:1
	v_mov_b32_dpp v3, v2 quad_perm:[2,3,0,1] row_mask:0xf bank_mask:0xf bound_ctrl:1
	v_mov_b32_dpp v5, v2 quad_perm:[3,2,1,0] row_mask:0xf bank_mask:0xf bound_ctrl:1
	s_and_saveexec_b64 s[12:13], s[2:3]
	s_cbranch_execz .LBB0_1056
	v_mov_b32_e32 v6, v203
	v_cvt_pk_fp8_f32 v6, v2, v4
	v_add_co_u32_e32 v2, vcc, 0x4000, v66
	v_cvt_pk_fp8_f32 v6, v3, v5 op_sel:[0,0,1]
	s_nop 0
	v_addc_co_u32_e32 v3, vcc, 0, v67, vcc
	ds_write_b32 v197, v6 offset:2400
.LBB0_1056:
	s_or_b64 exec, exec, s[12:13]
	ds_read_b32 v2, v1 offset:76
	s_waitcnt lgkmcnt(0)
	v_rcp_f32_e32 v2, v2
	s_nop 0
	v_mul_f32_e32 v2, 0x42000000, v2
	v_mul_f32_e32 v3, v61, v2
	s_nop 1
	v_mov_b32_dpp v5, v3 quad_perm:[1,0,3,2] row_mask:0xf bank_mask:0xf bound_ctrl:1
	v_mov_b32_dpp v4, v3 quad_perm:[2,3,0,1] row_mask:0xf bank_mask:0xf bound_ctrl:1
	v_mov_b32_dpp v6, v3 quad_perm:[3,2,1,0] row_mask:0xf bank_mask:0xf bound_ctrl:1
	s_and_saveexec_b64 s[12:13], s[2:3]
	s_cbranch_execz .LBB0_1058
	v_mov_b32_e32 v7, v203
	v_cvt_pk_fp8_f32 v7, v3, v5
	v_cvt_pk_fp8_f32 v7, v4, v6 op_sel:[0,0,1]
	v_add_co_u32_e32 v4, vcc, 0x4000, v66
	s_nop 1
	v_addc_co_u32_e32 v5, vcc, 0, v67, vcc
	ds_write_b32 v197, v7 offset:2432
.LBB0_1058:
	s_or_b64 exec, exec, s[12:13]
	v_mul_f32_e32 v3, v45, v2
	s_nop 1
	v_mov_b32_dpp v5, v3 quad_perm:[1,0,3,2] row_mask:0xf bank_mask:0xf bound_ctrl:1
	v_mov_b32_dpp v4, v3 quad_perm:[2,3,0,1] row_mask:0xf bank_mask:0xf bound_ctrl:1
	v_mov_b32_dpp v6, v3 quad_perm:[3,2,1,0] row_mask:0xf bank_mask:0xf bound_ctrl:1
	s_and_saveexec_b64 s[12:13], s[2:3]
	s_cbranch_execz .LBB0_1060
	v_mov_b32_e32 v7, v203
	v_cvt_pk_fp8_f32 v7, v3, v5
	v_cvt_pk_fp8_f32 v7, v4, v6 op_sel:[0,0,1]
	v_add_co_u32_e32 v4, vcc, 0x4000, v66
	s_nop 1
	v_addc_co_u32_e32 v5, vcc, 0, v67, vcc
	ds_write_b32 v197, v7 offset:2464
.LBB0_1060:
	s_or_b64 exec, exec, s[12:13]
	v_mul_f32_e32 v3, v29, v2
	s_nop 1
	v_mov_b32_dpp v5, v3 quad_perm:[1,0,3,2] row_mask:0xf bank_mask:0xf bound_ctrl:1
	v_mov_b32_dpp v4, v3 quad_perm:[2,3,0,1] row_mask:0xf bank_mask:0xf bound_ctrl:1
	v_mov_b32_dpp v6, v3 quad_perm:[3,2,1,0] row_mask:0xf bank_mask:0xf bound_ctrl:1
	s_and_saveexec_b64 s[12:13], s[2:3]
	s_cbranch_execz .LBB0_1062
	v_mov_b32_e32 v7, v203
	v_cvt_pk_fp8_f32 v7, v3, v5
	v_cvt_pk_fp8_f32 v7, v4, v6 op_sel:[0,0,1]
	v_add_co_u32_e32 v4, vcc, 0x4000, v66
	s_nop 1
	v_addc_co_u32_e32 v5, vcc, 0, v67, vcc
	ds_write_b32 v197, v7 offset:2496
.LBB0_1062:
	s_or_b64 exec, exec, s[12:13]
	v_mul_f32_e32 v2, v13, v2
	s_nop 1
	v_mov_b32_dpp v4, v2 quad_perm:[1,0,3,2] row_mask:0xf bank_mask:0xf bound_ctrl:1
	v_mov_b32_dpp v3, v2 quad_perm:[2,3,0,1] row_mask:0xf bank_mask:0xf bound_ctrl:1
	v_mov_b32_dpp v5, v2 quad_perm:[3,2,1,0] row_mask:0xf bank_mask:0xf bound_ctrl:1
	s_and_saveexec_b64 s[12:13], s[2:3]
	s_cbranch_execz .LBB0_1064
	v_mov_b32_e32 v6, v203
	v_cvt_pk_fp8_f32 v6, v2, v4
	v_add_co_u32_e32 v2, vcc, 0x4000, v66
	v_cvt_pk_fp8_f32 v6, v3, v5 op_sel:[0,0,1]
	s_nop 0
	v_addc_co_u32_e32 v3, vcc, 0, v67, vcc
	ds_write_b32 v197, v6 offset:2528
.LBB0_1064:
	s_or_b64 exec, exec, s[12:13]
	ds_read_b32 v2, v1 offset:96
	s_waitcnt lgkmcnt(0)
	v_rcp_f32_e32 v2, v2
	s_nop 0
	v_mul_f32_e32 v2, 0x42000000, v2
	v_mul_f32_e32 v3, v62, v2
	s_nop 1
	v_mov_b32_dpp v5, v3 quad_perm:[1,0,3,2] row_mask:0xf bank_mask:0xf bound_ctrl:1
	v_mov_b32_dpp v4, v3 quad_perm:[2,3,0,1] row_mask:0xf bank_mask:0xf bound_ctrl:1
	v_mov_b32_dpp v6, v3 quad_perm:[3,2,1,0] row_mask:0xf bank_mask:0xf bound_ctrl:1
	s_and_saveexec_b64 s[12:13], s[2:3]
	s_cbranch_execz .LBB0_1066
	v_mov_b32_e32 v7, v203
	v_cvt_pk_fp8_f32 v7, v3, v5
	v_cvt_pk_fp8_f32 v7, v4, v6 op_sel:[0,0,1]
	v_add_co_u32_e32 v4, vcc, 0x6000, v66
	s_nop 1
	v_addc_co_u32_e32 v5, vcc, 0, v67, vcc
	ds_write_b32 v197, v7 offset:3072
.LBB0_1066:
	s_or_b64 exec, exec, s[12:13]
	v_mul_f32_e32 v3, v46, v2
	s_nop 1
	v_mov_b32_dpp v5, v3 quad_perm:[1,0,3,2] row_mask:0xf bank_mask:0xf bound_ctrl:1
	v_mov_b32_dpp v4, v3 quad_perm:[2,3,0,1] row_mask:0xf bank_mask:0xf bound_ctrl:1
	v_mov_b32_dpp v6, v3 quad_perm:[3,2,1,0] row_mask:0xf bank_mask:0xf bound_ctrl:1
	s_and_saveexec_b64 s[12:13], s[2:3]
	s_cbranch_execz .LBB0_1068
	v_mov_b32_e32 v7, v203
	v_cvt_pk_fp8_f32 v7, v3, v5
	v_cvt_pk_fp8_f32 v7, v4, v6 op_sel:[0,0,1]
	v_add_co_u32_e32 v4, vcc, 0x6000, v66
	s_nop 1
	v_addc_co_u32_e32 v5, vcc, 0, v67, vcc
	ds_write_b32 v197, v7 offset:3104
.LBB0_1068:
	s_or_b64 exec, exec, s[12:13]
	v_mul_f32_e32 v3, v30, v2
	s_nop 1
	v_mov_b32_dpp v5, v3 quad_perm:[1,0,3,2] row_mask:0xf bank_mask:0xf bound_ctrl:1
	v_mov_b32_dpp v4, v3 quad_perm:[2,3,0,1] row_mask:0xf bank_mask:0xf bound_ctrl:1
	v_mov_b32_dpp v6, v3 quad_perm:[3,2,1,0] row_mask:0xf bank_mask:0xf bound_ctrl:1
	s_and_saveexec_b64 s[12:13], s[2:3]
	s_cbranch_execz .LBB0_1070
	v_mov_b32_e32 v7, v203
	v_cvt_pk_fp8_f32 v7, v3, v5
	v_cvt_pk_fp8_f32 v7, v4, v6 op_sel:[0,0,1]
	v_add_co_u32_e32 v4, vcc, 0x6000, v66
	s_nop 1
	v_addc_co_u32_e32 v5, vcc, 0, v67, vcc
	ds_write_b32 v197, v7 offset:3136
.LBB0_1070:
	s_or_b64 exec, exec, s[12:13]
	v_mul_f32_e32 v2, v14, v2
	s_nop 1
	v_mov_b32_dpp v4, v2 quad_perm:[1,0,3,2] row_mask:0xf bank_mask:0xf bound_ctrl:1
	v_mov_b32_dpp v3, v2 quad_perm:[2,3,0,1] row_mask:0xf bank_mask:0xf bound_ctrl:1
	v_mov_b32_dpp v5, v2 quad_perm:[3,2,1,0] row_mask:0xf bank_mask:0xf bound_ctrl:1
	s_and_saveexec_b64 s[12:13], s[2:3]
	s_cbranch_execz .LBB0_1072
	v_mov_b32_e32 v6, v203
	v_cvt_pk_fp8_f32 v6, v2, v4
	v_add_co_u32_e32 v2, vcc, 0x6000, v66
	v_cvt_pk_fp8_f32 v6, v3, v5 op_sel:[0,0,1]
	s_nop 0
	v_addc_co_u32_e32 v3, vcc, 0, v67, vcc
	ds_write_b32 v197, v6 offset:3168
.LBB0_1072:
	s_or_b64 exec, exec, s[12:13]
	ds_read_b32 v2, v1 offset:100
	s_waitcnt lgkmcnt(0)
	v_rcp_f32_e32 v2, v2
	s_nop 0
	v_mul_f32_e32 v2, 0x42000000, v2
	v_mul_f32_e32 v3, v63, v2
	s_nop 1
	v_mov_b32_dpp v5, v3 quad_perm:[1,0,3,2] row_mask:0xf bank_mask:0xf bound_ctrl:1
	v_mov_b32_dpp v4, v3 quad_perm:[2,3,0,1] row_mask:0xf bank_mask:0xf bound_ctrl:1
	v_mov_b32_dpp v6, v3 quad_perm:[3,2,1,0] row_mask:0xf bank_mask:0xf bound_ctrl:1
	s_and_saveexec_b64 s[12:13], s[2:3]
	s_cbranch_execz .LBB0_1074
	v_mov_b32_e32 v7, v203
	v_cvt_pk_fp8_f32 v7, v3, v5
	v_cvt_pk_fp8_f32 v7, v4, v6 op_sel:[0,0,1]
	v_add_co_u32_e32 v4, vcc, 0x6000, v66
	s_nop 1
	v_addc_co_u32_e32 v5, vcc, 0, v67, vcc
	ds_write_b32 v197, v7 offset:3200
.LBB0_1074:
	s_or_b64 exec, exec, s[12:13]
	v_mul_f32_e32 v3, v47, v2
	s_nop 1
	v_mov_b32_dpp v5, v3 quad_perm:[1,0,3,2] row_mask:0xf bank_mask:0xf bound_ctrl:1
	v_mov_b32_dpp v4, v3 quad_perm:[2,3,0,1] row_mask:0xf bank_mask:0xf bound_ctrl:1
	v_mov_b32_dpp v6, v3 quad_perm:[3,2,1,0] row_mask:0xf bank_mask:0xf bound_ctrl:1
	s_and_saveexec_b64 s[12:13], s[2:3]
	s_cbranch_execz .LBB0_1076
	v_mov_b32_e32 v7, v203
	v_cvt_pk_fp8_f32 v7, v3, v5
	v_cvt_pk_fp8_f32 v7, v4, v6 op_sel:[0,0,1]
	v_add_co_u32_e32 v4, vcc, 0x6000, v66
	s_nop 1
	v_addc_co_u32_e32 v5, vcc, 0, v67, vcc
	ds_write_b32 v197, v7 offset:3232
.LBB0_1076:
	s_or_b64 exec, exec, s[12:13]
	v_mul_f32_e32 v3, v31, v2
	s_nop 1
	v_mov_b32_dpp v5, v3 quad_perm:[1,0,3,2] row_mask:0xf bank_mask:0xf bound_ctrl:1
	v_mov_b32_dpp v4, v3 quad_perm:[2,3,0,1] row_mask:0xf bank_mask:0xf bound_ctrl:1
	v_mov_b32_dpp v6, v3 quad_perm:[3,2,1,0] row_mask:0xf bank_mask:0xf bound_ctrl:1
	s_and_saveexec_b64 s[12:13], s[2:3]
	s_cbranch_execz .LBB0_1078
	v_mov_b32_e32 v7, v203
	v_cvt_pk_fp8_f32 v7, v3, v5
	v_cvt_pk_fp8_f32 v7, v4, v6 op_sel:[0,0,1]
	v_add_co_u32_e32 v4, vcc, 0x6000, v66
	s_nop 1
	v_addc_co_u32_e32 v5, vcc, 0, v67, vcc
	ds_write_b32 v197, v7 offset:3264
.LBB0_1078:
	s_or_b64 exec, exec, s[12:13]
	v_mul_f32_e32 v2, v15, v2
	s_nop 1
	v_mov_b32_dpp v4, v2 quad_perm:[1,0,3,2] row_mask:0xf bank_mask:0xf bound_ctrl:1
	v_mov_b32_dpp v3, v2 quad_perm:[2,3,0,1] row_mask:0xf bank_mask:0xf bound_ctrl:1
	v_mov_b32_dpp v5, v2 quad_perm:[3,2,1,0] row_mask:0xf bank_mask:0xf bound_ctrl:1
	s_and_saveexec_b64 s[12:13], s[2:3]
	s_cbranch_execz .LBB0_1080
	v_mov_b32_e32 v6, v203
	v_cvt_pk_fp8_f32 v6, v2, v4
	v_add_co_u32_e32 v2, vcc, 0x6000, v66
	v_cvt_pk_fp8_f32 v6, v3, v5 op_sel:[0,0,1]
	s_nop 0
	v_addc_co_u32_e32 v3, vcc, 0, v67, vcc
	ds_write_b32 v197, v6 offset:3296
.LBB0_1080:
	s_or_b64 exec, exec, s[12:13]
	ds_read_b32 v2, v1 offset:104
	s_waitcnt lgkmcnt(0)
	v_rcp_f32_e32 v2, v2
	s_nop 0
	v_mul_f32_e32 v2, 0x42000000, v2
	v_mul_f32_e32 v3, v64, v2
	s_nop 1
	v_mov_b32_dpp v5, v3 quad_perm:[1,0,3,2] row_mask:0xf bank_mask:0xf bound_ctrl:1
	v_mov_b32_dpp v4, v3 quad_perm:[2,3,0,1] row_mask:0xf bank_mask:0xf bound_ctrl:1
	v_mov_b32_dpp v6, v3 quad_perm:[3,2,1,0] row_mask:0xf bank_mask:0xf bound_ctrl:1
	s_and_saveexec_b64 s[12:13], s[2:3]
	s_cbranch_execz .LBB0_1082
	v_mov_b32_e32 v7, v203
	v_cvt_pk_fp8_f32 v7, v3, v5
	v_cvt_pk_fp8_f32 v7, v4, v6 op_sel:[0,0,1]
	v_add_co_u32_e32 v4, vcc, 0x6000, v66
	s_nop 1
	v_addc_co_u32_e32 v5, vcc, 0, v67, vcc
	ds_write_b32 v197, v7 offset:3328
.LBB0_1082:
	s_or_b64 exec, exec, s[12:13]
	v_mul_f32_e32 v3, v48, v2
	s_nop 1
	v_mov_b32_dpp v5, v3 quad_perm:[1,0,3,2] row_mask:0xf bank_mask:0xf bound_ctrl:1
	v_mov_b32_dpp v4, v3 quad_perm:[2,3,0,1] row_mask:0xf bank_mask:0xf bound_ctrl:1
	v_mov_b32_dpp v6, v3 quad_perm:[3,2,1,0] row_mask:0xf bank_mask:0xf bound_ctrl:1
	s_and_saveexec_b64 s[12:13], s[2:3]
	s_cbranch_execz .LBB0_1084
	v_mov_b32_e32 v7, v203
	v_cvt_pk_fp8_f32 v7, v3, v5
	v_cvt_pk_fp8_f32 v7, v4, v6 op_sel:[0,0,1]
	v_add_co_u32_e32 v4, vcc, 0x6000, v66
	s_nop 1
	v_addc_co_u32_e32 v5, vcc, 0, v67, vcc
	ds_write_b32 v197, v7 offset:3360
.LBB0_1084:
	s_or_b64 exec, exec, s[12:13]
	v_mul_f32_e32 v3, v32, v2
	s_nop 1
	v_mov_b32_dpp v5, v3 quad_perm:[1,0,3,2] row_mask:0xf bank_mask:0xf bound_ctrl:1
	v_mov_b32_dpp v4, v3 quad_perm:[2,3,0,1] row_mask:0xf bank_mask:0xf bound_ctrl:1
	v_mov_b32_dpp v6, v3 quad_perm:[3,2,1,0] row_mask:0xf bank_mask:0xf bound_ctrl:1
	s_and_saveexec_b64 s[12:13], s[2:3]
	s_cbranch_execz .LBB0_1086
	v_mov_b32_e32 v7, v203
	v_cvt_pk_fp8_f32 v7, v3, v5
	v_cvt_pk_fp8_f32 v7, v4, v6 op_sel:[0,0,1]
	v_add_co_u32_e32 v4, vcc, 0x6000, v66
	s_nop 1
	v_addc_co_u32_e32 v5, vcc, 0, v67, vcc
	ds_write_b32 v197, v7 offset:3392
.LBB0_1086:
	s_or_b64 exec, exec, s[12:13]
	v_mul_f32_e32 v2, v16, v2
	s_nop 1
	v_mov_b32_dpp v4, v2 quad_perm:[1,0,3,2] row_mask:0xf bank_mask:0xf bound_ctrl:1
	v_mov_b32_dpp v3, v2 quad_perm:[2,3,0,1] row_mask:0xf bank_mask:0xf bound_ctrl:1
	v_mov_b32_dpp v5, v2 quad_perm:[3,2,1,0] row_mask:0xf bank_mask:0xf bound_ctrl:1
	s_and_saveexec_b64 s[12:13], s[2:3]
	s_cbranch_execz .LBB0_1088
	v_mov_b32_e32 v6, v203
	v_cvt_pk_fp8_f32 v6, v2, v4
	v_add_co_u32_e32 v2, vcc, 0x6000, v66
	v_cvt_pk_fp8_f32 v6, v3, v5 op_sel:[0,0,1]
	s_nop 0
	v_addc_co_u32_e32 v3, vcc, 0, v67, vcc
	ds_write_b32 v197, v6 offset:3424
.LBB0_1088:
	s_or_b64 exec, exec, s[12:13]
	ds_read_b32 v1, v1 offset:108
	s_waitcnt lgkmcnt(0)
	v_rcp_f32_e32 v1, v1
	s_nop 0
	v_mul_f32_e32 v1, 0x42000000, v1
	v_mul_f32_e32 v2, v65, v1
	s_nop 1
	v_mov_b32_dpp v4, v2 quad_perm:[1,0,3,2] row_mask:0xf bank_mask:0xf bound_ctrl:1
	v_mov_b32_dpp v3, v2 quad_perm:[2,3,0,1] row_mask:0xf bank_mask:0xf bound_ctrl:1
	v_mov_b32_dpp v5, v2 quad_perm:[3,2,1,0] row_mask:0xf bank_mask:0xf bound_ctrl:1
	s_and_saveexec_b64 s[12:13], s[2:3]
	s_cbranch_execz .LBB0_1090
	v_mov_b32_e32 v6, v203
	v_cvt_pk_fp8_f32 v6, v2, v4
	v_add_co_u32_e32 v2, vcc, 0x6000, v66
	v_cvt_pk_fp8_f32 v6, v3, v5 op_sel:[0,0,1]
	s_nop 0
	v_addc_co_u32_e32 v3, vcc, 0, v67, vcc
	ds_write_b32 v197, v6 offset:3456
.LBB0_1090:
	s_or_b64 exec, exec, s[12:13]
	v_mul_f32_e32 v2, v49, v1
	s_nop 1
	v_mov_b32_dpp v4, v2 quad_perm:[1,0,3,2] row_mask:0xf bank_mask:0xf bound_ctrl:1
	v_mov_b32_dpp v3, v2 quad_perm:[2,3,0,1] row_mask:0xf bank_mask:0xf bound_ctrl:1
	v_mov_b32_dpp v5, v2 quad_perm:[3,2,1,0] row_mask:0xf bank_mask:0xf bound_ctrl:1
	s_and_saveexec_b64 s[12:13], s[2:3]
	s_cbranch_execz .LBB0_1092
	v_mov_b32_e32 v6, v203
	v_cvt_pk_fp8_f32 v6, v2, v4
	v_add_co_u32_e32 v2, vcc, 0x6000, v66
	v_cvt_pk_fp8_f32 v6, v3, v5 op_sel:[0,0,1]
	s_nop 0
	v_addc_co_u32_e32 v3, vcc, 0, v67, vcc
	ds_write_b32 v197, v6 offset:3488
.LBB0_1092:
	s_or_b64 exec, exec, s[12:13]
	v_mul_f32_e32 v2, v33, v1
	s_nop 1
	v_mov_b32_dpp v4, v2 quad_perm:[1,0,3,2] row_mask:0xf bank_mask:0xf bound_ctrl:1
	v_mov_b32_dpp v3, v2 quad_perm:[2,3,0,1] row_mask:0xf bank_mask:0xf bound_ctrl:1
	v_mov_b32_dpp v5, v2 quad_perm:[3,2,1,0] row_mask:0xf bank_mask:0xf bound_ctrl:1
	s_and_saveexec_b64 s[12:13], s[2:3]
	s_cbranch_execz .LBB0_1094
	v_mov_b32_e32 v6, v203
	v_cvt_pk_fp8_f32 v6, v2, v4
	v_add_co_u32_e32 v2, vcc, 0x6000, v66
	v_cvt_pk_fp8_f32 v6, v3, v5 op_sel:[0,0,1]
	s_nop 0
	v_addc_co_u32_e32 v3, vcc, 0, v67, vcc
	ds_write_b32 v197, v6 offset:3520
.LBB0_1094:
	s_or_b64 exec, exec, s[12:13]
	v_mul_f32_e32 v1, v17, v1
	s_nop 1
	v_mov_b32_dpp v3, v1 quad_perm:[1,0,3,2] row_mask:0xf bank_mask:0xf bound_ctrl:1
	v_mov_b32_dpp v2, v1 quad_perm:[2,3,0,1] row_mask:0xf bank_mask:0xf bound_ctrl:1
	v_mov_b32_dpp v4, v1 quad_perm:[3,2,1,0] row_mask:0xf bank_mask:0xf bound_ctrl:1
	s_and_saveexec_b64 s[12:13], s[2:3]
	s_cbranch_execz .LBB0_938
	v_mov_b32_e32 v5, v203
	v_cvt_pk_fp8_f32 v5, v1, v3
	v_cvt_pk_fp8_f32 v5, v2, v4 op_sel:[0,0,1]
	v_add_co_u32_e32 v2, vcc, 0x6000, v66
	s_nop 1
	v_addc_co_u32_e32 v3, vcc, 0, v67, vcc
	ds_write_b32 v197, v5 offset:3552
	s_branch .LBB0_938
